# ogemm_v1
# speedup vs baseline: 1.0566x; 1.0012x over previous
.LBB2_3:
	s_load_dwordx4 s[4:7], s[0:1], 0x0
	s_load_dwordx2 s[8:9], s[0:1], 0x10
	v_and_b32_e32 v4, 15, v0
	v_lshrrev_b32_e32 v5, 6, v0
	s_and_b32 s10, s2, 0x70
	v_lshl_add_u32 v14, v5, 1, s10
	v_lshl_or_b32 v14, v14, 5, v4
	v_mov_b32_e32 v3, 0
	v_lshlrev_b32_e32 v26, 1, v0
	v_and_b32_e32 v26, 0x60, v26
	v_and_b32_e32 v2, 63, v0
	v_lshlrev_b32_e32 v2, 4, v2
	s_and_b32 s11, s2, 15
	v_lshlrev_b32_e32 v27, 12, v5
	v_lshl_or_b32 v16, s11, 17, v27
	v_or_b32_e32 v16, v16, v2
	v_lshlrev_b32_e32 v15, 8, v14
	v_or_b32_e32 v15, v15, v26
	v_lshlrev_b32_e32 v14, 3, v14
	v_add_u32_e32 v17, 0x1000, v15
	v_add_u32_e32 v12, 0x8000, v16
	v_add_u32_e32 v13, 0x10000, v16
	v_add_u32_e32 v6, 0x18000, v16
	v_add_u32_e32 v10, 0x2000, v15
	v_add_u32_e32 v11, 0x3000, v15
	s_mov_b32 s12, 0xff800000
	s_waitcnt lgkmcnt(0)
	global_load_dwordx2 v[18:19], v14, s[6:7]
	global_load_dwordx2 v[20:21], v14, s[6:7] offset:128
	global_load_dwordx2 v[22:23], v14, s[6:7] offset:256
	global_load_dwordx2 v[24:25], v14, s[6:7] offset:384
	global_load_dwordx4 v[32:35], v15, s[4:5]
	global_load_dwordx4 v[36:39], v15, s[4:5] offset:16
	global_load_dwordx4 v[40:43], v17, s[4:5]
	global_load_dwordx4 v[44:47], v17, s[4:5] offset:16
	global_load_dwordx4 v[48:51], v15, s[4:5] offset:128
	global_load_dwordx4 v[52:55], v15, s[4:5] offset:144
	global_load_dwordx4 v[56:59], v17, s[4:5] offset:128
	global_load_dwordx4 v[60:63], v17, s[4:5] offset:144
	global_load_dwordx4 v[64:67], v16, s[8:9]
	global_load_dwordx4 v[68:71], v16, s[8:9] offset:1024
	global_load_dwordx4 v[72:75], v16, s[8:9] offset:2048
	global_load_dwordx4 v[76:79], v16, s[8:9] offset:3072
	global_load_dwordx4 v[80:83], v12, s[8:9]
	global_load_dwordx4 v[84:87], v12, s[8:9] offset:1024
	global_load_dwordx4 v[88:91], v12, s[8:9] offset:2048
	global_load_dwordx4 v[92:95], v12, s[8:9] offset:3072
	global_load_dwordx4 v[96:99], v13, s[8:9]
	global_load_dwordx4 v[100:103], v13, s[8:9] offset:1024
	global_load_dwordx4 v[104:107], v13, s[8:9] offset:2048
	global_load_dwordx4 v[108:111], v13, s[8:9] offset:3072
	global_load_dwordx4 v[112:115], v6, s[8:9]
	global_load_dwordx4 v[116:119], v6, s[8:9] offset:1024
	global_load_dwordx4 v[120:123], v6, s[8:9] offset:2048
	global_load_dwordx4 v[124:127], v6, s[8:9] offset:3072
	s_waitcnt vmcnt(24)
	v_max3_f32 v26, v18, s12, v20
	v_max3_f32 v27, v22, s12, v24
	v_sub_f32_e32 v28, v18, v26
	v_sub_f32_e32 v29, v20, v26
	v_sub_f32_e32 v30, v22, v27
	v_sub_f32_e32 v31, v24, v27
	v_mul_f32_e32 v28, 0x3fb8aa3b, v28
	v_mul_f32_e32 v29, 0x3fb8aa3b, v29
	v_mul_f32_e32 v30, 0x3fb8aa3b, v30
	v_mul_f32_e32 v31, 0x3fb8aa3b, v31
	v_exp_f32_e32 v28, v28
	v_exp_f32_e32 v29, v29
	v_exp_f32_e32 v30, v30
	v_exp_f32_e32 v31, v31
	s_nop 0
	v_mul_f32_e32 v18, v19, v28
	v_mul_f32_e32 v20, v21, v29
	v_mul_f32_e32 v22, v23, v30
	v_mul_f32_e32 v24, v25, v31
	v_add_f32_e32 v18, 0, v18
	v_add_f32_e32 v22, 0, v22
	v_add_f32_e32 v19, v18, v20
	v_add_f32_e32 v23, v22, v24
	v_div_scale_f32 v18, s[14:15], v19, v19, 1.0
	v_div_scale_f32 v20, vcc, 1.0, v19, 1.0
	v_rcp_f32_e32 v21, v18
	s_nop 0
	v_fma_f32 v26, -v18, v21, 1.0
	v_fmac_f32_e32 v21, v26, v21
	v_mul_f32_e32 v27, v20, v21
	v_fma_f32 v26, -v18, v27, v20
	v_fmac_f32_e32 v27, v26, v21
	v_fma_f32 v26, -v18, v27, v20
	v_div_fmas_f32 v26, v26, v21, v27
	v_div_fixup_f32 v26, v26, v19, 1.0
	v_div_scale_f32 v22, s[14:15], v23, v23, 1.0
	v_div_scale_f32 v24, vcc, 1.0, v23, 1.0
	v_rcp_f32_e32 v25, v22
	s_nop 0
	v_fma_f32 v18, -v22, v25, 1.0
	v_fmac_f32_e32 v25, v18, v25
	v_mul_f32_e32 v20, v24, v25
	v_fma_f32 v18, -v22, v20, v24
	v_fmac_f32_e32 v20, v18, v25
	v_fma_f32 v18, -v22, v20, v24
	v_div_fmas_f32 v18, v18, v25, v20
	v_div_fixup_f32 v27, v18, v23, 1.0
	s_waitcnt vmcnt(20)
	v_mul_f32_e32 v32, v32, v28
	v_mul_f32_e32 v33, v33, v28
	v_mul_f32_e32 v34, v34, v28
	v_mul_f32_e32 v35, v35, v28
	v_mul_f32_e32 v36, v36, v28
	v_mul_f32_e32 v37, v37, v28
	v_mul_f32_e32 v38, v38, v28
	v_mul_f32_e32 v39, v39, v28
	v_fmac_f32_e32 v32, v40, v29
	v_fmac_f32_e32 v33, v41, v29
	v_fmac_f32_e32 v34, v42, v29
	v_fmac_f32_e32 v35, v43, v29
	v_fmac_f32_e32 v36, v44, v29
	v_fmac_f32_e32 v37, v45, v29
	v_fmac_f32_e32 v38, v46, v29
	v_fmac_f32_e32 v39, v47, v29
	v_mul_f32_e32 v32, v26, v32
	v_mul_f32_e32 v33, v26, v33
	v_mul_f32_e32 v34, v26, v34
	v_mul_f32_e32 v35, v26, v35
	v_mul_f32_e32 v36, v26, v36
	v_mul_f32_e32 v37, v26, v37
	v_mul_f32_e32 v38, v26, v38
	v_mul_f32_e32 v39, v26, v39
	v_cvt_pk_f16_f32 v6, v32, v33
	v_cvt_pk_f16_f32 v7, v34, v35
	v_cvt_pk_f16_f32 v8, v36, v37
	v_cvt_pk_f16_f32 v9, v38, v39
	s_waitcnt vmcnt(16)
	v_mul_f32_e32 v48, v48, v28
	v_mul_f32_e32 v49, v49, v28
	v_mul_f32_e32 v50, v50, v28
	v_mul_f32_e32 v51, v51, v28
	v_mul_f32_e32 v52, v52, v28
	v_mul_f32_e32 v53, v53, v28
	v_mul_f32_e32 v54, v54, v28
	v_mul_f32_e32 v55, v55, v28
	v_fmac_f32_e32 v48, v56, v29
	v_fmac_f32_e32 v49, v57, v29
	v_fmac_f32_e32 v50, v58, v29
	v_fmac_f32_e32 v51, v59, v29
	v_fmac_f32_e32 v52, v60, v29
	v_fmac_f32_e32 v53, v61, v29
	v_fmac_f32_e32 v54, v62, v29
	v_fmac_f32_e32 v55, v63, v29
	v_mul_f32_e32 v48, v26, v48
	v_mul_f32_e32 v49, v26, v49
	v_mul_f32_e32 v50, v26, v50
	v_mul_f32_e32 v51, v26, v51
	v_mul_f32_e32 v52, v26, v52
	v_mul_f32_e32 v53, v26, v53
	v_mul_f32_e32 v54, v26, v54
	v_mul_f32_e32 v55, v26, v55
	v_cvt_pk_f16_f32 v14, v48, v49
	v_cvt_pk_f16_f32 v15, v50, v51
	v_cvt_pk_f16_f32 v16, v52, v53
	v_cvt_pk_f16_f32 v17, v54, v55
	global_load_dwordx4 v[32:35], v10, s[4:5]
	global_load_dwordx4 v[36:39], v10, s[4:5] offset:16
	global_load_dwordx4 v[40:43], v11, s[4:5]
	global_load_dwordx4 v[44:47], v11, s[4:5] offset:16
	global_load_dwordx4 v[48:51], v10, s[4:5] offset:128
	global_load_dwordx4 v[52:55], v10, s[4:5] offset:144
	global_load_dwordx4 v[56:59], v11, s[4:5] offset:128
	global_load_dwordx4 v[60:63], v11, s[4:5] offset:144
	s_waitcnt vmcnt(4)
	v_mul_f32_e32 v32, v32, v30
	v_mul_f32_e32 v33, v33, v30
	v_mul_f32_e32 v34, v34, v30
	v_mul_f32_e32 v35, v35, v30
	v_mul_f32_e32 v36, v36, v30
	v_mul_f32_e32 v37, v37, v30
	v_mul_f32_e32 v38, v38, v30
	v_mul_f32_e32 v39, v39, v30
	v_fmac_f32_e32 v32, v40, v31
	v_fmac_f32_e32 v33, v41, v31
	v_fmac_f32_e32 v34, v42, v31
	v_fmac_f32_e32 v35, v43, v31
	v_fmac_f32_e32 v36, v44, v31
	v_fmac_f32_e32 v37, v45, v31
	v_fmac_f32_e32 v38, v46, v31
	v_fmac_f32_e32 v39, v47, v31
	v_mul_f32_e32 v32, v27, v32
	v_mul_f32_e32 v33, v27, v33
	v_mul_f32_e32 v34, v27, v34
	v_mul_f32_e32 v35, v27, v35
	v_mul_f32_e32 v36, v27, v36
	v_mul_f32_e32 v37, v27, v37
	v_mul_f32_e32 v38, v27, v38
	v_mul_f32_e32 v39, v27, v39
	v_cvt_pk_f16_f32 v18, v32, v33
	v_cvt_pk_f16_f32 v19, v34, v35
	v_cvt_pk_f16_f32 v20, v36, v37
	v_cvt_pk_f16_f32 v21, v38, v39
	s_waitcnt vmcnt(0)
	v_mul_f32_e32 v48, v48, v30
	v_mul_f32_e32 v49, v49, v30
	v_mul_f32_e32 v50, v50, v30
	v_mul_f32_e32 v51, v51, v30
	v_mul_f32_e32 v52, v52, v30
	v_mul_f32_e32 v53, v53, v30
	v_mul_f32_e32 v54, v54, v30
	v_mul_f32_e32 v55, v55, v30
	v_fmac_f32_e32 v48, v56, v31
	v_fmac_f32_e32 v49, v57, v31
	v_fmac_f32_e32 v50, v58, v31
	v_fmac_f32_e32 v51, v59, v31
	v_fmac_f32_e32 v52, v60, v31
	v_fmac_f32_e32 v53, v61, v31
	v_fmac_f32_e32 v54, v62, v31
	v_fmac_f32_e32 v55, v63, v31
	v_mul_f32_e32 v48, v27, v48
	v_mul_f32_e32 v49, v27, v49
	v_mul_f32_e32 v50, v27, v50
	v_mul_f32_e32 v51, v27, v51
	v_mul_f32_e32 v52, v27, v52
	v_mul_f32_e32 v53, v27, v53
	v_mul_f32_e32 v54, v27, v54
	v_mul_f32_e32 v55, v27, v55
	v_cvt_pk_f16_f32 v10, v48, v49
	v_cvt_pk_f16_f32 v11, v50, v51
	v_cvt_pk_f16_f32 v12, v52, v53
	v_cvt_pk_f16_f32 v13, v54, v55
	v_lshlrev_b32_e32 v5, 12, v5
	v_or_b32_e32 v5, v5, v2
	v_mfma_f32_16x16x32_f16 v[32:35], v[64:67], v[6:9], 0
	v_mfma_f32_16x16x32_f16 v[36:39], v[80:83], v[6:9], 0
	v_mfma_f32_16x16x32_f16 v[40:43], v[96:99], v[6:9], 0
	v_mfma_f32_16x16x32_f16 v[44:47], v[112:115], v[6:9], 0
	v_mfma_f32_16x16x32_f16 v[32:35], v[68:71], v[14:17], v[32:35]
	v_mfma_f32_16x16x32_f16 v[36:39], v[84:87], v[14:17], v[36:39]
	v_mfma_f32_16x16x32_f16 v[40:43], v[100:103], v[14:17], v[40:43]
	v_mfma_f32_16x16x32_f16 v[44:47], v[116:119], v[14:17], v[44:47]
	v_mfma_f32_16x16x32_f16 v[32:35], v[72:75], v[18:21], v[32:35]
	v_mfma_f32_16x16x32_f16 v[36:39], v[88:91], v[18:21], v[36:39]
	v_mfma_f32_16x16x32_f16 v[40:43], v[104:107], v[18:21], v[40:43]
	v_mfma_f32_16x16x32_f16 v[44:47], v[120:123], v[18:21], v[44:47]
	v_mfma_f32_16x16x32_f16 v[32:35], v[76:79], v[10:13], v[32:35]
	v_mfma_f32_16x16x32_f16 v[36:39], v[92:95], v[10:13], v[36:39]
	v_mfma_f32_16x16x32_f16 v[40:43], v[108:111], v[10:13], v[40:43]
	v_mfma_f32_16x16x32_f16 v[44:47], v[124:127], v[10:13], v[44:47]
	s_and_b32 s10, s2, 15
	v_cmp_gt_u32_e32 vcc, s3, v0
	s_nop 7
	s_nop 1
	ds_write_b128 v5, v[32:35]
	ds_write_b128 v5, v[36:39] offset:1024
	ds_write_b128 v5, v[40:43] offset:2048
	ds_write_b128 v5, v[44:47] offset:3072
	s_waitcnt lgkmcnt(0)
	s_barrier
	s_and_saveexec_b64 s[4:5], vcc
	s_cbranch_execz .LBB2_5
	v_lshlrev_b32_e32 v2, 4, v4
	v_lshl_or_b32 v2, v1, 9, v2
	ds_read_b128 v[6:9], v2
	ds_read_b128 v[10:13], v2 offset:4096
	ds_read_b128 v[14:17], v2 offset:256
	ds_read_b128 v[18:21], v2 offset:8192
	ds_read_b128 v[22:25], v2 offset:4352
	ds_read_b128 v[26:29], v2 offset:12288
	ds_read_b128 v[30:33], v2 offset:8448
	ds_read_b128 v[34:37], v2 offset:16384
	ds_read_b128 v[38:41], v2 offset:12544
	s_waitcnt lgkmcnt(8)
	v_pk_add_f32 v[6:7], v[6:7], 0 op_sel_hi:[1,0]
	v_pk_add_f32 v[8:9], v[8:9], 0 op_sel_hi:[1,0]
	s_waitcnt lgkmcnt(7)
	v_pk_add_f32 v[6:7], v[6:7], v[10:11]
	ds_read_b128 v[42:45], v2 offset:20480
	ds_read_b128 v[46:49], v2 offset:16640
	v_pk_add_f32 v[8:9], v[8:9], v[12:13]
	s_waitcnt lgkmcnt(7)
	v_pk_add_f32 v[6:7], v[6:7], v[18:19]
	v_pk_add_f32 v[8:9], v[8:9], v[20:21]
	s_waitcnt lgkmcnt(5)
	v_pk_add_f32 v[6:7], v[6:7], v[26:27]
	ds_read_b128 v[50:53], v2 offset:24576
	ds_read_b128 v[54:57], v2 offset:28672
	ds_read_b128 v[58:61], v2 offset:20736
	v_pk_add_f32 v[8:9], v[8:9], v[28:29]
	s_waitcnt lgkmcnt(6)
	v_pk_add_f32 v[6:7], v[6:7], v[34:35]
	v_pk_add_f32 v[8:9], v[8:9], v[36:37]
	s_waitcnt lgkmcnt(4)
	v_pk_add_f32 v[6:7], v[6:7], v[42:43]
	v_pk_add_f32 v[8:9], v[8:9], v[44:45]
	s_waitcnt lgkmcnt(2)
	v_pk_add_f32 v[6:7], v[6:7], v[50:51]
	v_pk_add_f32 v[8:9], v[8:9], v[52:53]
	s_waitcnt lgkmcnt(1)
	v_pk_add_f32 v[6:7], v[6:7], v[54:55]
	v_pk_add_f32 v[8:9], v[8:9], v[56:57]
	v_cvt_pk_f16_f32 v6, v6, v7
	v_cvt_pk_f16_f32 v7, v8, v9
	v_pk_add_f32 v[8:9], v[14:15], 0 op_sel_hi:[1,0]
	v_pk_add_f32 v[10:11], v[16:17], 0 op_sel_hi:[1,0]
	ds_read_b128 v[62:65], v2 offset:24832
	ds_read_b128 v[66:69], v2 offset:28928
	v_pk_add_f32 v[8:9], v[8:9], v[22:23]
	v_pk_add_f32 v[10:11], v[10:11], v[24:25]
	v_pk_add_f32 v[8:9], v[8:9], v[30:31]
	v_pk_add_f32 v[10:11], v[10:11], v[32:33]
	s_load_dwordx2 s[6:7], s[0:1], 0x18
	v_pk_add_f32 v[8:9], v[8:9], v[38:39]
	v_pk_add_f32 v[10:11], v[10:11], v[40:41]
	s_lshl_b32 s8, s10, 4
	v_lshlrev_b32_e32 v2, 1, v1
	s_lshr_b32 s3, s2, 4
	v_pk_add_f32 v[8:9], v[8:9], v[46:47]
	v_pk_add_f32 v[10:11], v[10:11], v[48:49]
	v_and_or_b32 v2, v2, 8, s8
	s_waitcnt lgkmcnt(0)
	v_pk_add_f32 v[8:9], v[8:9], v[58:59]
	v_pk_add_f32 v[10:11], v[10:11], v[60:61]
	v_or_b32_e32 v2, s3, v2
	v_pk_add_f32 v[8:9], v[8:9], v[62:63]
	v_pk_add_f32 v[10:11], v[10:11], v[64:65]
	v_lshlrev_b32_e32 v2, 6, v2
	v_and_b32_e32 v5, 48, v0
	v_pk_add_f32 v[8:9], v[8:9], v[66:67]
	v_pk_add_f32 v[10:11], v[10:11], v[68:69]
	v_or3_b32 v2, v2, v5, v4
	v_cvt_pk_f16_f32 v8, v8, v9
	v_cvt_pk_f16_f32 v9, v10, v11
	v_lshl_add_u64 v[2:3], v[2:3], 4, s[6:7]
	global_store_dwordx4 v[2:3], v[6:9], off

.LBB2_6:
	s_load_dword s3, s[0:1], 0x30
	s_load_dwordx4 s[4:7], s[0:1], 0x20
	v_lshlrev_b32_e32 v2, 4, v0
	v_and_b32_e32 v10, 0xf0, v2
	v_mov_b32_e32 v11, 0
	s_waitcnt lgkmcnt(0)
	s_add_i32 s0, s2, s3
	s_add_i32 s1, s0, 0xffffff80
	s_mul_hi_i32 s0, s1, 0x10624dd3
	s_lshr_b32 s2, s0, 31
	s_ashr_i32 s0, s0, 5
	s_add_i32 s0, s0, s2
	s_mul_i32 s2, s0, 0x1f4
	s_sub_i32 s1, s1, s2
	s_lshl_b32 s2, s1, 6
	s_ashr_i32 s3, s2, 31
	s_lshl_b32 s0, s0, 6
	s_lshl_b64 s[8:9], s[2:3], 2
	s_add_u32 s4, s4, s8
	s_addc_u32 s5, s5, s9
	v_lshl_add_u64 v[6:7], s[4:5], 0, v[10:11]
	v_or_b32_e32 v2, s0, v1
	s_mov_b32 s1, 0x1f400
	v_or_b32_e32 v8, 0x200, v0
	v_mad_i64_i32 v[2:3], s[4:5], v2, s1, v[6:7]
	v_lshrrev_b32_e32 v12, 4, v8
	global_load_dwordx4 v[2:5], v[2:3], off nt
	v_or_b32_e32 v8, s0, v12
	v_mad_i64_i32 v[6:7], s[4:5], v8, s1, v[6:7]
	global_load_dwordx4 v[6:9], v[6:7], off nt
	v_lshrrev_b32_e32 v13, 3, v0
	v_lshlrev_b32_e32 v0, 3, v0
	v_and_b32_e32 v14, 56, v0
	v_mul_u32_u24_e32 v0, 0x104, v14
	s_movk_i32 s1, 0x104
	v_lshl_add_u32 v16, v13, 2, v0
	v_or_b32_e32 v0, s2, v13
	v_mad_u32_u24 v15, v1, s1, v10
	v_ashrrev_i32_e32 v1, 31, v0
	v_lshlrev_b64 v[0:1], 11, v[0:1]
	v_mad_u32_u24 v10, v12, s1, v10
	v_add_u32_e32 v17, 0x400, v16
	v_lshl_add_u64 v[0:1], s[6:7], 0, v[0:1]
	s_ashr_i32 s1, s0, 31
	v_lshl_add_u64 v[12:13], s[0:1], 1, v[0:1]
	s_waitcnt vmcnt(1)
	ds_write2_b32 v15, v2, v3 offset1:1
	ds_write2_b32 v15, v4, v5 offset0:2 offset1:3
	s_waitcnt vmcnt(0)
	ds_write2_b32 v10, v6, v7 offset1:1
	ds_write2_b32 v10, v8, v9 offset0:2 offset1:3
	s_waitcnt lgkmcnt(0)
	s_barrier
	ds_read2_b32 v[0:1], v17 offset0:134 offset1:199
	ds_read2_b32 v[4:5], v17 offset0:4 offset1:69
	ds_read2_b32 v[6:7], v16 offset0:130 offset1:195
	ds_read2_b32 v[8:9], v16 offset1:65
	v_lshlrev_b32_e32 v10, 1, v14
	s_waitcnt lgkmcnt(3)
	v_cvt_pk_f16_f32 v3, v0, v1
	s_waitcnt lgkmcnt(2)
	v_cvt_pk_f16_f32 v2, v4, v5
	s_waitcnt lgkmcnt(1)
	v_cvt_pk_f16_f32 v1, v6, v7
	s_waitcnt lgkmcnt(0)
	v_cvt_pk_f16_f32 v0, v8, v9
	v_lshl_add_u64 v[4:5], v[12:13], 0, v[10:11]
	global_store_dwordx4 v[4:5], v[0:3], off
	s_endpgm
	s_nop 0
	s_nop 0
	s_nop 0
	s_nop 0
	s_nop 0
	s_nop 0
	s_nop 0
	s_nop 0
	s_nop 0
	s_nop 0
	s_nop 0
	s_nop 0
	s_nop 0
	s_nop 0
	s_nop 0
	s_nop 0
	s_nop 0
	s_nop 0
	s_nop 0
	s_nop 0
	s_nop 0
	s_nop 0
	s_nop 0
	s_nop 0
	s_nop 0
	s_nop 0
	s_nop 0
	s_nop 0
	s_nop 0
	s_nop 0
	s_endpgm

	.amdhsa_kernel _ZN12_GLOBAL__N_16o_gemmEPKfS1_PKDF16_PDF16_S1_S4_i
		.amdhsa_group_segment_fixed_size 32768
		.amdhsa_private_segment_fixed_size 0
		.amdhsa_kernarg_size 52
		.amdhsa_user_sgpr_count 2
		.amdhsa_user_sgpr_dispatch_ptr 0
		.amdhsa_user_sgpr_queue_ptr 0
		.amdhsa_user_sgpr_kernarg_segment_ptr 1
		.amdhsa_user_sgpr_dispatch_id 0
		.amdhsa_user_sgpr_kernarg_preload_length 0
		.amdhsa_user_sgpr_kernarg_preload_offset 0
		.amdhsa_user_sgpr_private_segment_size 0
		.amdhsa_uses_dynamic_stack 0
		.amdhsa_enable_private_segment 0
		.amdhsa_system_sgpr_workgroup_id_x 1
		.amdhsa_system_sgpr_workgroup_id_y 0
		.amdhsa_system_sgpr_workgroup_id_z 0
		.amdhsa_system_sgpr_workgroup_info 0
		.amdhsa_system_vgpr_workitem_id 0
		.amdhsa_next_free_vgpr 128
		.amdhsa_next_free_sgpr 16
		.amdhsa_accum_offset 128
		.amdhsa_reserve_vcc 1
		.amdhsa_float_round_mode_32 0
		.amdhsa_float_round_mode_16_64 0
		.amdhsa_float_denorm_mode_32 3
		.amdhsa_float_denorm_mode_16_64 3
		.amdhsa_dx10_clamp 1
		.amdhsa_ieee_mode 1
		.amdhsa_fp16_overflow 0
		.amdhsa_tg_split 0
		.amdhsa_exception_fp_ieee_invalid_op 0
		.amdhsa_exception_fp_denorm_src 0
		.amdhsa_exception_fp_ieee_div_zero 0
		.amdhsa_exception_fp_ieee_overflow 0
		.amdhsa_exception_fp_ieee_underflow 0
		.amdhsa_exception_fp_ieee_inexact 0
		.amdhsa_exception_int_div_zero 0
	.end_amdhsa_kernel

amdhsa.kernels:
  - .agpr_count:     0
    .args:
      - .actual_access:  read_only
        .address_space:  global
        .offset:         0
        .size:           8
        .value_kind:     global_buffer
      - .actual_access:  read_only
        .address_space:  global
        .offset:         8
        .size:           8
        .value_kind:     global_buffer
      - .actual_access:  read_only
        .address_space:  global
        .offset:         16
        .size:           8
        .value_kind:     global_buffer
      - .actual_access:  read_only
        .address_space:  global
        .offset:         24
        .size:           8
        .value_kind:     global_buffer
      - .actual_access:  read_only
        .address_space:  global
        .offset:         32
        .size:           8
        .value_kind:     global_buffer
      - .actual_access:  write_only
        .address_space:  global
        .offset:         40
        .size:           8
        .value_kind:     global_buffer
      - .actual_access:  write_only
        .address_space:  global
        .offset:         48
        .size:           8
        .value_kind:     global_buffer
    .group_segment_fixed_size: 34816
    .kernarg_segment_align: 8
    .kernarg_segment_size: 56
    .language:       OpenCL C
    .language_version:
      - 2
      - 0
    .max_flat_workgroup_size: 512
    .name:           _ZN12_GLOBAL__N_16attn_qEPKDF16_S1_PK15HIP_vector_typeIfLj2EEPKhS7_PfS8_
    .private_segment_fixed_size: 0
    .sgpr_count:     30
    .sgpr_spill_count: 0
    .symbol:         _ZN12_GLOBAL__N_16attn_qEPKDF16_S1_PK15HIP_vector_typeIfLj2EEPKhS7_PfS8_.kd
    .uniform_work_group_size: 1
    .uses_dynamic_stack: false
    .vgpr_count:     172
    .vgpr_spill_count: 0
    .wavefront_size: 64
  - .agpr_count:     0
    .args:
      - .actual_access:  read_only
        .address_space:  global
        .offset:         0
        .size:           8
        .value_kind:     global_buffer
      - .actual_access:  read_only
        .address_space:  global
        .offset:         8
        .size:           8
        .value_kind:     global_buffer
      - .actual_access:  write_only
        .address_space:  global
        .offset:         16
        .size:           8
        .value_kind:     global_buffer
      - .actual_access:  read_only
        .address_space:  global
        .offset:         24
        .size:           8
        .value_kind:     global_buffer
      - .actual_access:  write_only
        .address_space:  global
        .offset:         32
        .size:           8
        .value_kind:     global_buffer
      - .actual_access:  read_only
        .address_space:  global
        .offset:         40
        .size:           8
        .value_kind:     global_buffer
      - .actual_access:  write_only
        .address_space:  global
        .offset:         48
        .size:           8
        .value_kind:     global_buffer
      - .actual_access:  read_only
        .address_space:  global
        .offset:         56
        .size:           8
        .value_kind:     global_buffer
      - .actual_access:  write_only
        .address_space:  global
        .offset:         64
        .size:           8
        .value_kind:     global_buffer
      - .actual_access:  read_only
        .address_space:  global
        .offset:         72
        .size:           8
        .value_kind:     global_buffer
      - .actual_access:  write_only
        .address_space:  global
        .offset:         80
        .size:           8
        .value_kind:     global_buffer
      - .actual_access:  read_only
        .address_space:  global
        .offset:         88
        .size:           8
        .value_kind:     global_buffer
      - .actual_access:  write_only
        .address_space:  global
        .offset:         96
        .size:           8
        .value_kind:     global_buffer
      - .actual_access:  write_only
        .address_space:  global
        .offset:         104
        .size:           8
        .value_kind:     global_buffer
      - .actual_access:  read_only
        .address_space:  global
        .offset:         112
        .size:           8
        .value_kind:     global_buffer
      - .actual_access:  write_only
        .address_space:  global
        .offset:         120
        .size:           8
        .value_kind:     global_buffer
      - .actual_access:  write_only
        .address_space:  global
        .offset:         128
        .size:           8
        .value_kind:     global_buffer
      - .actual_access:  read_only
        .address_space:  global
        .offset:         136
        .size:           8
        .value_kind:     global_buffer
      - .actual_access:  read_only
        .address_space:  global
        .offset:         144
        .size:           8
        .value_kind:     global_buffer
      - .actual_access:  write_only
        .address_space:  global
        .offset:         152
        .size:           8
        .value_kind:     global_buffer
      - .actual_access:  read_only
        .address_space:  global
        .offset:         160
        .size:           8
        .value_kind:     global_buffer
      - .actual_access:  read_only
        .address_space:  global
        .offset:         168
        .size:           8
        .value_kind:     global_buffer
      - .actual_access:  read_only
        .address_space:  global
        .offset:         176
        .size:           8
        .value_kind:     global_buffer
      - .actual_access:  write_only
        .address_space:  global
        .offset:         184
        .size:           8
        .value_kind:     global_buffer
      - .actual_access:  write_only
        .address_space:  global
        .offset:         192
        .size:           8
        .value_kind:     global_buffer
    .group_segment_fixed_size: 16640
    .kernarg_segment_align: 8
    .kernarg_segment_size: 200
    .language:       OpenCL C
    .language_version:
      - 2
      - 0
    .max_flat_workgroup_size: 256
    .name:           _ZN12_GLOBAL__N_18prep_allEPKiPKfPDF16_S3_S4_S3_S4_S3_S4_S3_S4_S3_S4_P15HIP_vector_typeIfLj2EES3_PfS4_S1_S1_S4_S3_S3_S3_S8_S8_
    .private_segment_fixed_size: 0
    .sgpr_count:     24
    .sgpr_spill_count: 0
    .symbol:         _ZN12_GLOBAL__N_18prep_allEPKiPKfPDF16_S3_S4_S3_S4_S3_S4_S3_S4_S3_S4_P15HIP_vector_typeIfLj2EES3_PfS4_S1_S1_S4_S3_S3_S3_S8_S8_.kd
    .uniform_work_group_size: 1
    .uses_dynamic_stack: false
    .vgpr_count:     35
    .vgpr_spill_count: 0
    .wavefront_size: 64
  - .agpr_count:     0
    .args:
      - .actual_access:  read_only
        .address_space:  global
        .offset:         0
        .size:           8
        .value_kind:     global_buffer
      - .actual_access:  read_only
        .address_space:  global
        .offset:         8
        .size:           8
        .value_kind:     global_buffer
      - .actual_access:  read_only
        .address_space:  global
        .offset:         16
        .size:           8
        .value_kind:     global_buffer
      - .actual_access:  write_only
        .address_space:  global
        .offset:         24
        .size:           8
        .value_kind:     global_buffer
      - .actual_access:  read_only
        .address_space:  global
        .offset:         32
        .size:           8
        .value_kind:     global_buffer
      - .actual_access:  write_only
        .address_space:  global
        .offset:         40
        .size:           8
        .value_kind:     global_buffer
      - .offset:         48
        .size:           4
        .value_kind:     by_value
    .group_segment_fixed_size: 32768
    .kernarg_segment_align: 8
    .kernarg_segment_size: 52
    .language:       OpenCL C
    .language_version:
      - 2
      - 0
    .max_flat_workgroup_size: 512
    .name:           _ZN12_GLOBAL__N_16o_gemmEPKfS1_PKDF16_PDF16_S1_S4_i
    .private_segment_fixed_size: 0
    .sgpr_count:     22
    .sgpr_spill_count: 0
    .symbol:         _ZN12_GLOBAL__N_16o_gemmEPKfS1_PKDF16_PDF16_S1_S4_i.kd
    .uniform_work_group_size: 1
    .uses_dynamic_stack: false
    .vgpr_count:     128
    .vgpr_spill_count: 0
    .wavefront_size: 64
  - .agpr_count:     0
    .args:
      - .actual_access:  read_only
        .address_space:  global
        .offset:         0
        .size:           8
        .value_kind:     global_buffer
      - .offset:         8
        .size:           4
        .value_kind:     by_value
      - .offset:         12
        .size:           4
        .value_kind:     by_value
      - .actual_access:  read_only
        .address_space:  global
        .offset:         16
        .size:           8
        .value_kind:     global_buffer
      - .actual_access:  read_only
        .address_space:  global
        .offset:         24
        .size:           8
        .value_kind:     global_buffer
      - .actual_access:  read_only
        .address_space:  global
        .offset:         32
        .size:           8
        .value_kind:     global_buffer
      - .actual_access:  write_only
        .address_space:  global
        .offset:         40
        .size:           8
        .value_kind:     global_buffer
      - .actual_access:  read_only
        .address_space:  global
        .offset:         48
        .size:           8
        .value_kind:     global_buffer
      - .actual_access:  write_only
        .address_space:  global
        .offset:         56
        .size:           8
        .value_kind:     global_buffer
      - .offset:         64
        .size:           4
        .value_kind:     by_value
    .group_segment_fixed_size: 0
    .kernarg_segment_align: 8
    .kernarg_segment_size: 68
    .language:       OpenCL C
    .language_version:
      - 2
      - 0
    .max_flat_workgroup_size: 1024
    .name:           _ZN12_GLOBAL__N_113sync_a_kernelEPKfiiPKiS3_S1_PDF16_S1_S4_i
    .private_segment_fixed_size: 0
    .sgpr_count:     33
    .sgpr_spill_count: 0
    .symbol:         _ZN12_GLOBAL__N_113sync_a_kernelEPKfiiPKiS3_S1_PDF16_S1_S4_i.kd
    .uniform_work_group_size: 1
    .uses_dynamic_stack: false
    .vgpr_count:     49
    .vgpr_spill_count: 0
    .wavefront_size: 64
  - .agpr_count:     0
    .args:
      - .actual_access:  read_only
        .address_space:  global
        .offset:         0
        .size:           8
        .value_kind:     global_buffer
      - .actual_access:  read_only
        .address_space:  global
        .offset:         8
        .size:           8
        .value_kind:     global_buffer
      - .actual_access:  write_only
        .address_space:  global
        .offset:         16
        .size:           8
        .value_kind:     global_buffer
      - .offset:         24
        .size:           4
        .value_kind:     by_value
      - .actual_access:  read_only
        .address_space:  global
        .offset:         32
        .size:           8
        .value_kind:     global_buffer
      - .actual_access:  read_only
        .address_space:  global
        .offset:         40
        .size:           8
        .value_kind:     global_buffer
      - .actual_access:  read_only
        .address_space:  global
        .offset:         48
        .size:           8
        .value_kind:     global_buffer
      - .actual_access:  write_only
        .address_space:  global
        .offset:         56
        .size:           8
        .value_kind:     global_buffer
    .group_segment_fixed_size: 8192
    .kernarg_segment_align: 8
    .kernarg_segment_size: 64
    .language:       OpenCL C
    .language_version:
      - 2
      - 0
    .max_flat_workgroup_size: 1024
    .name:           _ZN12_GLOBAL__N_110sync_a_incEPKfS1_PfiPKiS4_S1_PDF16_
    .private_segment_fixed_size: 0
    .sgpr_count:     24
    .sgpr_spill_count: 0
    .symbol:         _ZN12_GLOBAL__N_110sync_a_incEPKfS1_PfiPKiS4_S1_PDF16_.kd
    .uniform_work_group_size: 1
    .uses_dynamic_stack: false
    .vgpr_count:     14
    .vgpr_spill_count: 0
    .wavefront_size: 64
  - .agpr_count:     0
    .args:
      - .actual_access:  read_only
        .address_space:  global
        .offset:         0
        .size:           8
        .value_kind:     global_buffer
      - .actual_access:  read_only
        .address_space:  global
        .offset:         8
        .size:           8
        .value_kind:     global_buffer
      - .actual_access:  read_only
        .address_space:  global
        .offset:         16
        .size:           8
        .value_kind:     global_buffer
      - .actual_access:  read_only
        .address_space:  global
        .offset:         24
        .size:           8
        .value_kind:     global_buffer
      - .actual_access:  write_only
        .address_space:  global
        .offset:         32
        .size:           8
        .value_kind:     global_buffer
    .group_segment_fixed_size: 0
    .kernarg_segment_align: 8
    .kernarg_segment_size: 40
    .language:       OpenCL C
    .language_version:
      - 2
      - 0
    .max_flat_workgroup_size: 1024
    .name:           _ZN12_GLOBAL__N_110sync_o_allEPKfPKiS3_S1_PDF16_
    .private_segment_fixed_size: 0
    .sgpr_count:     18
    .sgpr_spill_count: 0
    .symbol:         _ZN12_GLOBAL__N_110sync_o_allEPKfPKiS3_S1_PDF16_.kd
    .uniform_work_group_size: 1
    .uses_dynamic_stack: false
    .vgpr_count:     33
    .vgpr_spill_count: 0
    .wavefront_size: 64
  - .agpr_count:     0
    .args:
      - .address_space:  global
        .offset:         0
        .size:           8
        .value_kind:     global_buffer
      - .address_space:  global
        .offset:         8
        .size:           8
        .value_kind:     global_buffer
      - .offset:         16
        .size:           4
        .value_kind:     by_value
      - .offset:         20
        .size:           4
        .value_kind:     by_value
      - .actual_access:  read_only
        .address_space:  global
        .offset:         24
        .size:           8
        .value_kind:     global_buffer
      - .actual_access:  write_only
        .address_space:  global
        .offset:         32
        .size:           8
        .value_kind:     global_buffer
      - .actual_access:  write_only
        .address_space:  global
        .offset:         40
        .size:           8
        .value_kind:     global_buffer
      - .actual_access:  read_only
        .address_space:  global
        .offset:         48
        .size:           8
        .value_kind:     global_buffer
      - .actual_access:  read_only
        .address_space:  global
        .offset:         56
        .size:           8
        .value_kind:     global_buffer
    .group_segment_fixed_size: 0
    .kernarg_segment_align: 8
    .kernarg_segment_size: 64
    .language:       OpenCL C
    .language_version:
      - 2
      - 0
    .max_flat_workgroup_size: 512
    .name:           _ZN12_GLOBAL__N_18big_gemmILi0EEEvPKDF16_S2_iiPK15HIP_vector_typeIfLj2EEPhS7_PKfPf
    .private_segment_fixed_size: 0
    .sgpr_count:     50
    .sgpr_spill_count: 0
    .symbol:         _ZN12_GLOBAL__N_18big_gemmILi0EEEvPKDF16_S2_iiPK15HIP_vector_typeIfLj2EEPhS7_PKfPf.kd
    .uniform_work_group_size: 1
    .uses_dynamic_stack: false
    .vgpr_count:     255
    .vgpr_spill_count: 0
    .wavefront_size: 64
  - .agpr_count:     0
    .args:
      - .address_space:  global
        .offset:         0
        .size:           8
        .value_kind:     global_buffer
      - .address_space:  global
        .offset:         8
        .size:           8
        .value_kind:     global_buffer
      - .offset:         16
        .size:           4
        .value_kind:     by_value
      - .offset:         20
        .size:           4
        .value_kind:     by_value
      - .actual_access:  read_only
        .address_space:  global
        .offset:         24
        .size:           8
        .value_kind:     global_buffer
      - .actual_access:  read_only
        .address_space:  global
        .offset:         32
        .size:           8
        .value_kind:     global_buffer
      - .actual_access:  read_only
        .address_space:  global
        .offset:         40
        .size:           8
        .value_kind:     global_buffer
      - .actual_access:  read_only
        .address_space:  global
        .offset:         48
        .size:           8
        .value_kind:     global_buffer
      - .actual_access:  write_only
        .address_space:  global
        .offset:         56
        .size:           8
        .value_kind:     global_buffer
    .group_segment_fixed_size: 0
    .kernarg_segment_align: 8
    .kernarg_segment_size: 64
    .language:       OpenCL C
    .language_version:
      - 2
      - 0
    .max_flat_workgroup_size: 512
    .name:           _ZN12_GLOBAL__N_18big_gemmILi1EEEvPKDF16_S2_iiPK15HIP_vector_typeIfLj2EEPhS7_PKfPf
    .private_segment_fixed_size: 0
    .sgpr_count:     49
    .sgpr_spill_count: 0
    .symbol:         _ZN12_GLOBAL__N_18big_gemmILi1EEEvPKDF16_S2_iiPK15HIP_vector_typeIfLj2EEPhS7_PKfPf.kd
    .uniform_work_group_size: 1
    .uses_dynamic_stack: false
    .vgpr_count:     234
    .vgpr_spill_count: 0
    .wavefront_size: 64
  - .agpr_count:     0
    .args:
      - .actual_access:  read_only
        .address_space:  global
        .offset:         0
        .size:           8
        .value_kind:     global_buffer
      - .actual_access:  read_only
        .address_space:  global
        .offset:         8
        .size:           8
        .value_kind:     global_buffer
      - .actual_access:  read_only
        .address_space:  global
        .offset:         16
        .size:           8
        .value_kind:     global_buffer
      - .actual_access:  write_only
        .address_space:  global
        .offset:         24
        .size:           8
        .value_kind:     global_buffer
      - .actual_access:  read_only
        .address_space:  global
        .offset:         32
        .size:           8
        .value_kind:     global_buffer
      - .actual_access:  read_only
        .address_space:  global
        .offset:         40
        .size:           8
        .value_kind:     global_buffer
      - .actual_access:  read_only
        .address_space:  global
        .offset:         48
        .size:           8
        .value_kind:     global_buffer
      - .actual_access:  read_only
        .address_space:  global
        .offset:         56
        .size:           8
        .value_kind:     global_buffer
      - .actual_access:  read_only
        .address_space:  global
        .offset:         64
        .size:           8
        .value_kind:     global_buffer
      - .actual_access:  read_only
        .address_space:  global
        .offset:         72
        .size:           8
        .value_kind:     global_buffer
      - .actual_access:  read_only
        .address_space:  global
        .offset:         80
        .size:           8
        .value_kind:     global_buffer
      - .actual_access:  read_only
        .address_space:  global
        .offset:         88
        .size:           8
        .value_kind:     global_buffer
    .group_segment_fixed_size: 0
    .kernarg_segment_align: 8
    .kernarg_segment_size: 96
    .language:       OpenCL C
    .language_version:
      - 2
      - 0
    .max_flat_workgroup_size: 512
    .name:           _ZN12_GLOBAL__N_110gemm_fullkILi0ELi0EEEvPKDF16_S2_PKfPDF16_PfS6_S4_S4_S4_S4_S4_S5_
    .private_segment_fixed_size: 0
    .sgpr_count:     20
    .sgpr_spill_count: 0
    .symbol:         _ZN12_GLOBAL__N_110gemm_fullkILi0ELi0EEEvPKDF16_S2_PKfPDF16_PfS6_S4_S4_S4_S4_S4_S5_.kd
    .uniform_work_group_size: 1
    .uses_dynamic_stack: false
    .vgpr_count:     231
    .vgpr_spill_count: 0
    .wavefront_size: 64
  - .agpr_count:     0
    .args:
      - .actual_access:  read_only
        .address_space:  global
        .offset:         0
        .size:           8
        .value_kind:     global_buffer
      - .actual_access:  read_only
        .address_space:  global
        .offset:         8
        .size:           8
        .value_kind:     global_buffer
      - .actual_access:  read_only
        .address_space:  global
        .offset:         16
        .size:           8
        .value_kind:     global_buffer
      - .actual_access:  read_only
        .address_space:  global
        .offset:         24
        .size:           8
        .value_kind:     global_buffer
      - .address_space:  global
        .offset:         32
        .size:           8
        .value_kind:     global_buffer
      - .actual_access:  write_only
        .address_space:  global
        .offset:         40
        .size:           8
        .value_kind:     global_buffer
      - .actual_access:  read_only
        .address_space:  global
        .offset:         48
        .size:           8
        .value_kind:     global_buffer
      - .actual_access:  read_only
        .address_space:  global
        .offset:         56
        .size:           8
        .value_kind:     global_buffer
      - .actual_access:  read_only
        .address_space:  global
        .offset:         64
        .size:           8
        .value_kind:     global_buffer
      - .actual_access:  read_only
        .address_space:  global
        .offset:         72
        .size:           8
        .value_kind:     global_buffer
      - .actual_access:  read_only
        .address_space:  global
        .offset:         80
        .size:           8
        .value_kind:     global_buffer
      - .actual_access:  write_only
        .address_space:  global
        .offset:         88
        .size:           8
        .value_kind:     global_buffer
    .group_segment_fixed_size: 0
    .kernarg_segment_align: 8
    .kernarg_segment_size: 96
    .language:       OpenCL C
    .language_version:
      - 2
      - 0
    .max_flat_workgroup_size: 512
    .name:           _ZN12_GLOBAL__N_110gemm_fullkILi1ELi0EEEvPKDF16_S2_PKfPDF16_PfS6_S4_S4_S4_S4_S4_S5_
    .private_segment_fixed_size: 0
    .sgpr_count:     24
    .sgpr_spill_count: 0
    .symbol:         _ZN12_GLOBAL__N_110gemm_fullkILi1ELi0EEEvPKDF16_S2_PKfPDF16_PfS6_S4_S4_S4_S4_S4_S5_.kd
    .uniform_work_group_size: 1
    .uses_dynamic_stack: false
    .vgpr_count:     175
    .vgpr_spill_count: 0
    .wavefront_size: 64
  - .agpr_count:     0
    .args:
      - .actual_access:  read_only
        .address_space:  global
        .offset:         0
        .size:           8
        .value_kind:     global_buffer
      - .actual_access:  read_only
        .address_space:  global
        .offset:         8
        .size:           8
        .value_kind:     global_buffer
      - .actual_access:  read_only
        .address_space:  global
        .offset:         16
        .size:           8
        .value_kind:     global_buffer
      - .actual_access:  write_only
        .address_space:  global
        .offset:         24
        .size:           8
        .value_kind:     global_buffer
      - .actual_access:  read_only
        .address_space:  global
        .offset:         32
        .size:           8
        .value_kind:     global_buffer
      - .actual_access:  read_only
        .address_space:  global
        .offset:         40
        .size:           8
        .value_kind:     global_buffer
      - .actual_access:  read_only
        .address_space:  global
        .offset:         48
        .size:           8
        .value_kind:     global_buffer
      - .actual_access:  read_only
        .address_space:  global
        .offset:         56
        .size:           8
        .value_kind:     global_buffer
      - .actual_access:  read_only
        .address_space:  global
        .offset:         64
        .size:           8
        .value_kind:     global_buffer
      - .actual_access:  read_only
        .address_space:  global
        .offset:         72
        .size:           8
        .value_kind:     global_buffer
      - .actual_access:  read_only
        .address_space:  global
        .offset:         80
        .size:           8
        .value_kind:     global_buffer
      - .actual_access:  read_only
        .address_space:  global
        .offset:         88
        .size:           8
        .value_kind:     global_buffer
    .group_segment_fixed_size: 0
    .kernarg_segment_align: 8
    .kernarg_segment_size: 96
    .language:       OpenCL C
    .language_version:
      - 2
      - 0
    .max_flat_workgroup_size: 512
    .name:           _ZN12_GLOBAL__N_110gemm_fullkILi0ELi1EEEvPKDF16_S2_PKfPDF16_PfS6_S4_S4_S4_S4_S4_S5_
    .private_segment_fixed_size: 0
    .sgpr_count:     20
    .sgpr_spill_count: 0
    .symbol:         _ZN12_GLOBAL__N_110gemm_fullkILi0ELi1EEEvPKDF16_S2_PKfPDF16_PfS6_S4_S4_S4_S4_S4_S5_.kd
    .uniform_work_group_size: 1
    .uses_dynamic_stack: false
    .vgpr_count:     231
    .vgpr_spill_count: 0
    .wavefront_size: 64
  - .agpr_count:     0
    .args:
      - .actual_access:  read_only
        .address_space:  global
        .offset:         0
        .size:           8
        .value_kind:     global_buffer
      - .actual_access:  read_only
        .address_space:  global
        .offset:         8
        .size:           8
        .value_kind:     global_buffer
      - .actual_access:  read_only
        .address_space:  global
        .offset:         16
        .size:           8
        .value_kind:     global_buffer
      - .actual_access:  read_only
        .address_space:  global
        .offset:         24
        .size:           8
        .value_kind:     global_buffer
      - .address_space:  global
        .offset:         32
        .size:           8
        .value_kind:     global_buffer
      - .address_space:  global
        .offset:         40
        .size:           8
        .value_kind:     global_buffer
      - .actual_access:  read_only
        .address_space:  global
        .offset:         48
        .size:           8
        .value_kind:     global_buffer
      - .actual_access:  read_only
        .address_space:  global
        .offset:         56
        .size:           8
        .value_kind:     global_buffer
      - .actual_access:  read_only
        .address_space:  global
        .offset:         64
        .size:           8
        .value_kind:     global_buffer
      - .actual_access:  read_only
        .address_space:  global
        .offset:         72
        .size:           8
        .value_kind:     global_buffer
      - .actual_access:  read_only
        .address_space:  global
        .offset:         80
        .size:           8
        .value_kind:     global_buffer
      - .actual_access:  write_only
        .address_space:  global
        .offset:         88
        .size:           8
        .value_kind:     global_buffer
    .group_segment_fixed_size: 0
    .kernarg_segment_align: 8
    .kernarg_segment_size: 96
    .language:       OpenCL C
    .language_version:
      - 2
      - 0
    .max_flat_workgroup_size: 512
    .name:           _ZN12_GLOBAL__N_110gemm_fullkILi1ELi1EEEvPKDF16_S2_PKfPDF16_PfS6_S4_S4_S4_S4_S4_S5_
    .private_segment_fixed_size: 0
    .sgpr_count:     24
    .sgpr_spill_count: 0
    .symbol:         _ZN12_GLOBAL__N_110gemm_fullkILi1ELi1EEEvPKDF16_S2_PKfPDF16_PfS6_S4_S4_S4_S4_S4_S5_.kd
    .uniform_work_group_size: 1
    .uses_dynamic_stack: false
    .vgpr_count:     177
    .vgpr_spill_count: 0
    .wavefront_size: 64
  - .agpr_count:     0
    .args:
      - .actual_access:  read_only
        .address_space:  global
        .offset:         0
        .size:           8
        .value_kind:     global_buffer
      - .actual_access:  read_only
        .address_space:  global
        .offset:         8
        .size:           8
        .value_kind:     global_buffer
      - .actual_access:  read_only
        .address_space:  global
        .offset:         16
        .size:           8
        .value_kind:     global_buffer
      - .actual_access:  write_only
        .address_space:  global
        .offset:         24
        .size:           8
        .value_kind:     global_buffer
      - .actual_access:  read_only
        .address_space:  global
        .offset:         32
        .size:           8
        .value_kind:     global_buffer
      - .actual_access:  read_only
        .address_space:  global
        .offset:         40
        .size:           8
        .value_kind:     global_buffer
      - .actual_access:  read_only
        .address_space:  global
        .offset:         48
        .size:           8
        .value_kind:     global_buffer
      - .actual_access:  read_only
        .address_space:  global
        .offset:         56
        .size:           8
        .value_kind:     global_buffer
      - .actual_access:  read_only
        .address_space:  global
        .offset:         64
        .size:           8
        .value_kind:     global_buffer
      - .actual_access:  read_only
        .address_space:  global
        .offset:         72
        .size:           8
        .value_kind:     global_buffer
      - .actual_access:  read_only
        .address_space:  global
        .offset:         80
        .size:           8
        .value_kind:     global_buffer
      - .actual_access:  read_only
        .address_space:  global
        .offset:         88
        .size:           8
        .value_kind:     global_buffer
    .group_segment_fixed_size: 0
    .kernarg_segment_align: 8
    .kernarg_segment_size: 96
    .language:       OpenCL C
    .language_version:
      - 2
      - 0
    .max_flat_workgroup_size: 512
    .name:           _ZN12_GLOBAL__N_110gemm_fullkILi0ELi2EEEvPKDF16_S2_PKfPDF16_PfS6_S4_S4_S4_S4_S4_S5_
    .private_segment_fixed_size: 0
    .sgpr_count:     20
    .sgpr_spill_count: 0
    .symbol:         _ZN12_GLOBAL__N_110gemm_fullkILi0ELi2EEEvPKDF16_S2_PKfPDF16_PfS6_S4_S4_S4_S4_S4_S5_.kd
    .uniform_work_group_size: 1
    .uses_dynamic_stack: false
    .vgpr_count:     231
    .vgpr_spill_count: 0
    .wavefront_size: 64
  - .agpr_count:     0
    .args:
      - .actual_access:  read_only
        .address_space:  global
        .offset:         0
        .size:           8
        .value_kind:     global_buffer
      - .actual_access:  read_only
        .address_space:  global
        .offset:         8
        .size:           8
        .value_kind:     global_buffer
      - .actual_access:  read_only
        .address_space:  global
        .offset:         16
        .size:           8
        .value_kind:     global_buffer
      - .actual_access:  read_only
        .address_space:  global
        .offset:         24
        .size:           8
        .value_kind:     global_buffer
      - .address_space:  global
        .offset:         32
        .size:           8
        .value_kind:     global_buffer
      - .address_space:  global
        .offset:         40
        .size:           8
        .value_kind:     global_buffer
      - .actual_access:  read_only
        .address_space:  global
        .offset:         48
        .size:           8
        .value_kind:     global_buffer
      - .actual_access:  read_only
        .address_space:  global
        .offset:         56
        .size:           8
        .value_kind:     global_buffer
      - .actual_access:  read_only
        .address_space:  global
        .offset:         64
        .size:           8
        .value_kind:     global_buffer
      - .actual_access:  read_only
        .address_space:  global
        .offset:         72
        .size:           8
        .value_kind:     global_buffer
      - .actual_access:  read_only
        .address_space:  global
        .offset:         80
        .size:           8
        .value_kind:     global_buffer
      - .actual_access:  write_only
        .address_space:  global
        .offset:         88
        .size:           8
        .value_kind:     global_buffer
    .group_segment_fixed_size: 0
    .kernarg_segment_align: 8
    .kernarg_segment_size: 96
    .language:       OpenCL C
    .language_version:
      - 2
      - 0
    .max_flat_workgroup_size: 512
    .name:           _ZN12_GLOBAL__N_110gemm_fullkILi1ELi2EEEvPKDF16_S2_PKfPDF16_PfS6_S4_S4_S4_S4_S4_S5_
    .private_segment_fixed_size: 0
    .sgpr_count:     24
    .sgpr_spill_count: 0
    .symbol:         _ZN12_GLOBAL__N_110gemm_fullkILi1ELi2EEEvPKDF16_S2_PKfPDF16_PfS6_S4_S4_S4_S4_S4_S5_.kd
    .uniform_work_group_size: 1
    .uses_dynamic_stack: false
    .vgpr_count:     177
    .vgpr_spill_count: 0
    .wavefront_size: 64
  - .agpr_count:     0
    .args:
      - .actual_access:  read_only
        .address_space:  global
        .offset:         0
        .size:           8
        .value_kind:     global_buffer
      - .actual_access:  read_only
        .address_space:  global
        .offset:         8
        .size:           8
        .value_kind:     global_buffer
      - .actual_access:  read_only
        .address_space:  global
        .offset:         16
        .size:           8
        .value_kind:     global_buffer
      - .actual_access:  write_only
        .address_space:  global
        .offset:         24
        .size:           8
        .value_kind:     global_buffer
      - .actual_access:  read_only
        .address_space:  global
        .offset:         32
        .size:           8
        .value_kind:     global_buffer
      - .actual_access:  read_only
        .address_space:  global
        .offset:         40
        .size:           8
        .value_kind:     global_buffer
      - .actual_access:  read_only
        .address_space:  global
        .offset:         48
        .size:           8
        .value_kind:     global_buffer
      - .actual_access:  read_only
        .address_space:  global
        .offset:         56
        .size:           8
        .value_kind:     global_buffer
      - .actual_access:  read_only
        .address_space:  global
        .offset:         64
        .size:           8
        .value_kind:     global_buffer
      - .actual_access:  read_only
        .address_space:  global
        .offset:         72
        .size:           8
        .value_kind:     global_buffer
      - .actual_access:  read_only
        .address_space:  global
        .offset:         80
        .size:           8
        .value_kind:     global_buffer
      - .actual_access:  read_only
        .address_space:  global
        .offset:         88
        .size:           8
        .value_kind:     global_buffer
    .group_segment_fixed_size: 0
    .kernarg_segment_align: 8
    .kernarg_segment_size: 96
    .language:       OpenCL C
    .language_version:
      - 2
      - 0
    .max_flat_workgroup_size: 512
    .name:           _ZN12_GLOBAL__N_110gemm_fullkILi0ELi3EEEvPKDF16_S2_PKfPDF16_PfS6_S4_S4_S4_S4_S4_S5_
    .private_segment_fixed_size: 0
    .sgpr_count:     20
    .sgpr_spill_count: 0
    .symbol:         _ZN12_GLOBAL__N_110gemm_fullkILi0ELi3EEEvPKDF16_S2_PKfPDF16_PfS6_S4_S4_S4_S4_S4_S5_.kd
    .uniform_work_group_size: 1
    .uses_dynamic_stack: false
    .vgpr_count:     231
    .vgpr_spill_count: 0
    .wavefront_size: 64
  - .agpr_count:     0
    .args:
      - .actual_access:  read_only
        .address_space:  global
        .offset:         0
        .size:           8
        .value_kind:     global_buffer
      - .actual_access:  read_only
        .address_space:  global
        .offset:         8
        .size:           8
        .value_kind:     global_buffer
      - .actual_access:  read_only
        .address_space:  global
        .offset:         16
        .size:           8
        .value_kind:     global_buffer
      - .actual_access:  read_only
        .address_space:  global
        .offset:         24
        .size:           8
        .value_kind:     global_buffer
      - .address_space:  global
        .offset:         32
        .size:           8
        .value_kind:     global_buffer
      - .address_space:  global
        .offset:         40
        .size:           8
        .value_kind:     global_buffer
      - .actual_access:  read_only
        .address_space:  global
        .offset:         48
        .size:           8
        .value_kind:     global_buffer
      - .actual_access:  read_only
        .address_space:  global
        .offset:         56
        .size:           8
        .value_kind:     global_buffer
      - .actual_access:  read_only
        .address_space:  global
        .offset:         64
        .size:           8
        .value_kind:     global_buffer
      - .actual_access:  read_only
        .address_space:  global
        .offset:         72
        .size:           8
        .value_kind:     global_buffer
      - .actual_access:  read_only
        .address_space:  global
        .offset:         80
        .size:           8
        .value_kind:     global_buffer
      - .actual_access:  write_only
        .address_space:  global
        .offset:         88
        .size:           8
        .value_kind:     global_buffer
    .group_segment_fixed_size: 0
    .kernarg_segment_align: 8
    .kernarg_segment_size: 96
    .language:       OpenCL C
    .language_version:
      - 2
      - 0
    .max_flat_workgroup_size: 512
    .name:           _ZN12_GLOBAL__N_110gemm_fullkILi1ELi3EEEvPKDF16_S2_PKfPDF16_PfS6_S4_S4_S4_S4_S4_S5_
    .private_segment_fixed_size: 0
    .sgpr_count:     24
    .sgpr_spill_count: 0
    .symbol:         _ZN12_GLOBAL__N_110gemm_fullkILi1ELi3EEEvPKDF16_S2_PKfPDF16_PfS6_S4_S4_S4_S4_S4_S5_.kd
    .uniform_work_group_size: 1
    .uses_dynamic_stack: false
    .vgpr_count:     179
    .vgpr_spill_count: 0
    .wavefront_size: 64
  - .agpr_count:     0
    .args:
      - .actual_access:  read_only
        .address_space:  global
        .offset:         0
        .size:           8
        .value_kind:     global_buffer
      - .actual_access:  read_only
        .address_space:  global
        .offset:         8
        .size:           8
        .value_kind:     global_buffer
      - .actual_access:  read_only
        .address_space:  global
        .offset:         16
        .size:           8
        .value_kind:     global_buffer
      - .actual_access:  write_only
        .address_space:  global
        .offset:         24
        .size:           8
        .value_kind:     global_buffer
      - .actual_access:  read_only
        .address_space:  global
        .offset:         32
        .size:           8
        .value_kind:     global_buffer
      - .actual_access:  read_only
        .address_space:  global
        .offset:         40
        .size:           8
        .value_kind:     global_buffer
      - .actual_access:  read_only
        .address_space:  global
        .offset:         48
        .size:           8
        .value_kind:     global_buffer
      - .actual_access:  read_only
        .address_space:  global
        .offset:         56
        .size:           8
        .value_kind:     global_buffer
      - .actual_access:  read_only
        .address_space:  global
        .offset:         64
        .size:           8
        .value_kind:     global_buffer
      - .actual_access:  read_only
        .address_space:  global
        .offset:         72
        .size:           8
        .value_kind:     global_buffer
      - .actual_access:  read_only
        .address_space:  global
        .offset:         80
        .size:           8
        .value_kind:     global_buffer
      - .actual_access:  read_only
        .address_space:  global
        .offset:         88
        .size:           8
        .value_kind:     global_buffer
    .group_segment_fixed_size: 0
    .kernarg_segment_align: 8
    .kernarg_segment_size: 96
    .language:       OpenCL C
    .language_version:
      - 2
      - 0
    .max_flat_workgroup_size: 512
    .name:           _ZN12_GLOBAL__N_110gemm_fullkILi0ELi4EEEvPKDF16_S2_PKfPDF16_PfS6_S4_S4_S4_S4_S4_S5_
    .private_segment_fixed_size: 0
    .sgpr_count:     20
    .sgpr_spill_count: 0
    .symbol:         _ZN12_GLOBAL__N_110gemm_fullkILi0ELi4EEEvPKDF16_S2_PKfPDF16_PfS6_S4_S4_S4_S4_S4_S5_.kd
    .uniform_work_group_size: 1
    .uses_dynamic_stack: false
    .vgpr_count:     231
    .vgpr_spill_count: 0
    .wavefront_size: 64
  - .agpr_count:     0
    .args:
      - .actual_access:  read_only
        .address_space:  global
        .offset:         0
        .size:           8
        .value_kind:     global_buffer
      - .actual_access:  read_only
        .address_space:  global
        .offset:         8
        .size:           8
        .value_kind:     global_buffer
      - .actual_access:  read_only
        .address_space:  global
        .offset:         16
        .size:           8
        .value_kind:     global_buffer
      - .actual_access:  read_only
        .address_space:  global
        .offset:         24
        .size:           8
        .value_kind:     global_buffer
      - .address_space:  global
        .offset:         32
        .size:           8
        .value_kind:     global_buffer
      - .address_space:  global
        .offset:         40
        .size:           8
        .value_kind:     global_buffer
      - .actual_access:  read_only
        .address_space:  global
        .offset:         48
        .size:           8
        .value_kind:     global_buffer
      - .actual_access:  read_only
        .address_space:  global
        .offset:         56
        .size:           8
        .value_kind:     global_buffer
      - .actual_access:  read_only
        .address_space:  global
        .offset:         64
        .size:           8
        .value_kind:     global_buffer
      - .actual_access:  read_only
        .address_space:  global
        .offset:         72
        .size:           8
        .value_kind:     global_buffer
      - .actual_access:  read_only
        .address_space:  global
        .offset:         80
        .size:           8
        .value_kind:     global_buffer
      - .actual_access:  write_only
        .address_space:  global
        .offset:         88
        .size:           8
        .value_kind:     global_buffer
    .group_segment_fixed_size: 0
    .kernarg_segment_align: 8
    .kernarg_segment_size: 96
    .language:       OpenCL C
    .language_version:
      - 2
      - 0
    .max_flat_workgroup_size: 512
    .name:           _ZN12_GLOBAL__N_110gemm_fullkILi1ELi4EEEvPKDF16_S2_PKfPDF16_PfS6_S4_S4_S4_S4_S4_S5_
    .private_segment_fixed_size: 0
    .sgpr_count:     24
    .sgpr_spill_count: 0
    .symbol:         _ZN12_GLOBAL__N_110gemm_fullkILi1ELi4EEEvPKDF16_S2_PKfPDF16_PfS6_S4_S4_S4_S4_S4_S5_.kd
    .uniform_work_group_size: 1
    .uses_dynamic_stack: false
    .vgpr_count:     181
    .vgpr_spill_count: 0
    .wavefront_size: 64
  - .agpr_count:     0
    .args:
      - .actual_access:  read_only
        .address_space:  global
        .offset:         0
        .size:           8
        .value_kind:     global_buffer
      - .actual_access:  read_only
        .address_space:  global
        .offset:         8
        .size:           8
        .value_kind:     global_buffer
      - .actual_access:  read_only
        .address_space:  global
        .offset:         16
        .size:           8
        .value_kind:     global_buffer
      - .actual_access:  write_only
        .address_space:  global
        .offset:         24
        .size:           8
        .value_kind:     global_buffer
      - .actual_access:  read_only
        .address_space:  global
        .offset:         32
        .size:           8
        .value_kind:     global_buffer
      - .actual_access:  read_only
        .address_space:  global
        .offset:         40
        .size:           8
        .value_kind:     global_buffer
      - .actual_access:  read_only
        .address_space:  global
        .offset:         48
        .size:           8
        .value_kind:     global_buffer
      - .actual_access:  read_only
        .address_space:  global
        .offset:         56
        .size:           8
        .value_kind:     global_buffer
      - .actual_access:  read_only
        .address_space:  global
        .offset:         64
        .size:           8
        .value_kind:     global_buffer
      - .actual_access:  read_only
        .address_space:  global
        .offset:         72
        .size:           8
        .value_kind:     global_buffer
      - .actual_access:  read_only
        .address_space:  global
        .offset:         80
        .size:           8
        .value_kind:     global_buffer
      - .actual_access:  read_only
        .address_space:  global
        .offset:         88
        .size:           8
        .value_kind:     global_buffer
    .group_segment_fixed_size: 0
    .kernarg_segment_align: 8
    .kernarg_segment_size: 96
    .language:       OpenCL C
    .language_version:
      - 2
      - 0
    .max_flat_workgroup_size: 512
    .name:           _ZN12_GLOBAL__N_110gemm_fullkILi0ELi5EEEvPKDF16_S2_PKfPDF16_PfS6_S4_S4_S4_S4_S4_S5_
    .private_segment_fixed_size: 0
    .sgpr_count:     20
    .sgpr_spill_count: 0
    .symbol:         _ZN12_GLOBAL__N_110gemm_fullkILi0ELi5EEEvPKDF16_S2_PKfPDF16_PfS6_S4_S4_S4_S4_S4_S5_.kd
    .uniform_work_group_size: 1
    .uses_dynamic_stack: false
    .vgpr_count:     231
    .vgpr_spill_count: 0
    .wavefront_size: 64
  - .agpr_count:     0
    .args:
      - .actual_access:  read_only
        .address_space:  global
        .offset:         0
        .size:           8
        .value_kind:     global_buffer
      - .actual_access:  read_only
        .address_space:  global
        .offset:         8
        .size:           8
        .value_kind:     global_buffer
      - .actual_access:  read_only
        .address_space:  global
        .offset:         16
        .size:           8
        .value_kind:     global_buffer
      - .actual_access:  read_only
        .address_space:  global
        .offset:         24
        .size:           8
        .value_kind:     global_buffer
      - .address_space:  global
        .offset:         32
        .size:           8
        .value_kind:     global_buffer
      - .address_space:  global
        .offset:         40
        .size:           8
        .value_kind:     global_buffer
      - .actual_access:  read_only
        .address_space:  global
        .offset:         48
        .size:           8
        .value_kind:     global_buffer
      - .actual_access:  read_only
        .address_space:  global
        .offset:         56
        .size:           8
        .value_kind:     global_buffer
      - .actual_access:  read_only
        .address_space:  global
        .offset:         64
        .size:           8
        .value_kind:     global_buffer
      - .actual_access:  read_only
        .address_space:  global
        .offset:         72
        .size:           8
        .value_kind:     global_buffer
      - .actual_access:  read_only
        .address_space:  global
        .offset:         80
        .size:           8
        .value_kind:     global_buffer
      - .actual_access:  write_only
        .address_space:  global
        .offset:         88
        .size:           8
        .value_kind:     global_buffer
    .group_segment_fixed_size: 0
    .kernarg_segment_align: 8
    .kernarg_segment_size: 96
    .language:       OpenCL C
    .language_version:
      - 2
      - 0
    .max_flat_workgroup_size: 512
    .name:           _ZN12_GLOBAL__N_110gemm_fullkILi1ELi5EEEvPKDF16_S2_PKfPDF16_PfS6_S4_S4_S4_S4_S4_S5_
    .private_segment_fixed_size: 0
    .sgpr_count:     24
    .sgpr_spill_count: 0
    .symbol:         _ZN12_GLOBAL__N_110gemm_fullkILi1ELi5EEEvPKDF16_S2_PKfPDF16_PfS6_S4_S4_S4_S4_S4_S5_.kd
    .uniform_work_group_size: 1
    .uses_dynamic_stack: false
    .vgpr_count:     183
    .vgpr_spill_count: 0
    .wavefront_size: 64
  - .agpr_count:     0
    .args:
      - .actual_access:  read_only
        .address_space:  global
        .offset:         0
        .size:           8
        .value_kind:     global_buffer
      - .actual_access:  read_only
        .address_space:  global
        .offset:         8
        .size:           8
        .value_kind:     global_buffer
      - .actual_access:  read_only
        .address_space:  global
        .offset:         16
        .size:           8
        .value_kind:     global_buffer
      - .actual_access:  write_only
        .address_space:  global
        .offset:         24
        .size:           8
        .value_kind:     global_buffer
      - .actual_access:  read_only
        .address_space:  global
        .offset:         32
        .size:           8
        .value_kind:     global_buffer
      - .actual_access:  read_only
        .address_space:  global
        .offset:         40
        .size:           8
        .value_kind:     global_buffer
      - .actual_access:  read_only
        .address_space:  global
        .offset:         48
        .size:           8
        .value_kind:     global_buffer
      - .actual_access:  read_only
        .address_space:  global
        .offset:         56
        .size:           8
        .value_kind:     global_buffer
      - .actual_access:  read_only
        .address_space:  global
        .offset:         64
        .size:           8
        .value_kind:     global_buffer
      - .actual_access:  read_only
        .address_space:  global
        .offset:         72
        .size:           8
        .value_kind:     global_buffer
      - .actual_access:  read_only
        .address_space:  global
        .offset:         80
        .size:           8
        .value_kind:     global_buffer
      - .actual_access:  read_only
        .address_space:  global
        .offset:         88
        .size:           8
        .value_kind:     global_buffer
    .group_segment_fixed_size: 0
    .kernarg_segment_align: 8
    .kernarg_segment_size: 96
    .language:       OpenCL C
    .language_version:
      - 2
      - 0
    .max_flat_workgroup_size: 512
    .name:           _ZN12_GLOBAL__N_110gemm_fullkILi0ELi6EEEvPKDF16_S2_PKfPDF16_PfS6_S4_S4_S4_S4_S4_S5_
    .private_segment_fixed_size: 0
    .sgpr_count:     20
    .sgpr_spill_count: 0
    .symbol:         _ZN12_GLOBAL__N_110gemm_fullkILi0ELi6EEEvPKDF16_S2_PKfPDF16_PfS6_S4_S4_S4_S4_S4_S5_.kd
    .uniform_work_group_size: 1
    .uses_dynamic_stack: false
    .vgpr_count:     231
    .vgpr_spill_count: 0
    .wavefront_size: 64
  - .agpr_count:     0
    .args:
      - .actual_access:  read_only
        .address_space:  global
        .offset:         0
        .size:           8
        .value_kind:     global_buffer
      - .actual_access:  read_only
        .address_space:  global
        .offset:         8
        .size:           8
        .value_kind:     global_buffer
      - .actual_access:  read_only
        .address_space:  global
        .offset:         16
        .size:           8
        .value_kind:     global_buffer
      - .actual_access:  read_only
        .address_space:  global
        .offset:         24
        .size:           8
        .value_kind:     global_buffer
      - .address_space:  global
        .offset:         32
        .size:           8
        .value_kind:     global_buffer
      - .address_space:  global
        .offset:         40
        .size:           8
        .value_kind:     global_buffer
      - .actual_access:  read_only
        .address_space:  global
        .offset:         48
        .size:           8
        .value_kind:     global_buffer
      - .actual_access:  read_only
        .address_space:  global
        .offset:         56
        .size:           8
        .value_kind:     global_buffer
      - .actual_access:  read_only
        .address_space:  global
        .offset:         64
        .size:           8
        .value_kind:     global_buffer
      - .actual_access:  read_only
        .address_space:  global
        .offset:         72
        .size:           8
        .value_kind:     global_buffer
      - .actual_access:  read_only
        .address_space:  global
        .offset:         80
        .size:           8
        .value_kind:     global_buffer
      - .actual_access:  write_only
        .address_space:  global
        .offset:         88
        .size:           8
        .value_kind:     global_buffer
    .group_segment_fixed_size: 0
    .kernarg_segment_align: 8
    .kernarg_segment_size: 96
    .language:       OpenCL C
    .language_version:
      - 2
      - 0
    .max_flat_workgroup_size: 512
    .name:           _ZN12_GLOBAL__N_110gemm_fullkILi1ELi6EEEvPKDF16_S2_PKfPDF16_PfS6_S4_S4_S4_S4_S4_S5_
    .private_segment_fixed_size: 0
    .sgpr_count:     24
    .sgpr_spill_count: 0
    .symbol:         _ZN12_GLOBAL__N_110gemm_fullkILi1ELi6EEEvPKDF16_S2_PKfPDF16_PfS6_S4_S4_S4_S4_S4_S5_.kd
    .uniform_work_group_size: 1
    .uses_dynamic_stack: false
    .vgpr_count:     185
    .vgpr_spill_count: 0
    .wavefront_size: 64
  - .agpr_count:     0
    .args:
      - .actual_access:  read_only
        .address_space:  global
        .offset:         0
        .size:           8
        .value_kind:     global_buffer
      - .actual_access:  read_only
        .address_space:  global
        .offset:         8
        .size:           8
        .value_kind:     global_buffer
      - .actual_access:  read_only
        .address_space:  global
        .offset:         16
        .size:           8
        .value_kind:     global_buffer
      - .actual_access:  write_only
        .address_space:  global
        .offset:         24
        .size:           8
        .value_kind:     global_buffer
      - .actual_access:  read_only
        .address_space:  global
        .offset:         32
        .size:           8
        .value_kind:     global_buffer
      - .actual_access:  read_only
        .address_space:  global
        .offset:         40
        .size:           8
        .value_kind:     global_buffer
      - .actual_access:  read_only
        .address_space:  global
        .offset:         48
        .size:           8
        .value_kind:     global_buffer
      - .actual_access:  read_only
        .address_space:  global
        .offset:         56
        .size:           8
        .value_kind:     global_buffer
      - .actual_access:  read_only
        .address_space:  global
        .offset:         64
        .size:           8
        .value_kind:     global_buffer
      - .actual_access:  read_only
        .address_space:  global
        .offset:         72
        .size:           8
        .value_kind:     global_buffer
      - .actual_access:  read_only
        .address_space:  global
        .offset:         80
        .size:           8
        .value_kind:     global_buffer
      - .actual_access:  read_only
        .address_space:  global
        .offset:         88
        .size:           8
        .value_kind:     global_buffer
    .group_segment_fixed_size: 0
    .kernarg_segment_align: 8
    .kernarg_segment_size: 96
    .language:       OpenCL C
    .language_version:
      - 2
      - 0
    .max_flat_workgroup_size: 512
    .name:           _ZN12_GLOBAL__N_110gemm_fullkILi0ELi7EEEvPKDF16_S2_PKfPDF16_PfS6_S4_S4_S4_S4_S4_S5_
    .private_segment_fixed_size: 0
    .sgpr_count:     20
    .sgpr_spill_count: 0
    .symbol:         _ZN12_GLOBAL__N_110gemm_fullkILi0ELi7EEEvPKDF16_S2_PKfPDF16_PfS6_S4_S4_S4_S4_S4_S5_.kd
    .uniform_work_group_size: 1
    .uses_dynamic_stack: false
    .vgpr_count:     231
    .vgpr_spill_count: 0
    .wavefront_size: 64
  - .agpr_count:     0
    .args:
      - .actual_access:  read_only
        .address_space:  global
        .offset:         0
        .size:           8
        .value_kind:     global_buffer
      - .actual_access:  read_only
        .address_space:  global
        .offset:         8
        .size:           8
        .value_kind:     global_buffer
      - .actual_access:  read_only
        .address_space:  global
        .offset:         16
        .size:           8
        .value_kind:     global_buffer
      - .actual_access:  read_only
        .address_space:  global
        .offset:         24
        .size:           8
        .value_kind:     global_buffer
      - .address_space:  global
        .offset:         32
        .size:           8
        .value_kind:     global_buffer
      - .address_space:  global
        .offset:         40
        .size:           8
        .value_kind:     global_buffer
      - .actual_access:  read_only
        .address_space:  global
        .offset:         48
        .size:           8
        .value_kind:     global_buffer
      - .actual_access:  read_only
        .address_space:  global
        .offset:         56
        .size:           8
        .value_kind:     global_buffer
      - .actual_access:  read_only
        .address_space:  global
        .offset:         64
        .size:           8
        .value_kind:     global_buffer
      - .actual_access:  read_only
        .address_space:  global
        .offset:         72
        .size:           8
        .value_kind:     global_buffer
      - .actual_access:  read_only
        .address_space:  global
        .offset:         80
        .size:           8
        .value_kind:     global_buffer
      - .actual_access:  write_only
        .address_space:  global
        .offset:         88
        .size:           8
        .value_kind:     global_buffer
    .group_segment_fixed_size: 0
    .kernarg_segment_align: 8
    .kernarg_segment_size: 96
    .language:       OpenCL C
    .language_version:
      - 2
      - 0
    .max_flat_workgroup_size: 512
    .name:           _ZN12_GLOBAL__N_110gemm_fullkILi1ELi7EEEvPKDF16_S2_PKfPDF16_PfS6_S4_S4_S4_S4_S4_S5_
    .private_segment_fixed_size: 0
    .sgpr_count:     24
    .sgpr_spill_count: 0
    .symbol:         _ZN12_GLOBAL__N_110gemm_fullkILi1ELi7EEEvPKDF16_S2_PKfPDF16_PfS6_S4_S4_S4_S4_S4_S5_.kd
    .uniform_work_group_size: 1
    .uses_dynamic_stack: false
    .vgpr_count:     187
    .vgpr_spill_count: 0
    .wavefront_size: 64
